# baseline (speedup 1.0000x reference)
.LBB0_60:
	s_or_b64 exec, exec, s[8:9]
	v_add_f32_e32 v1, v6, v7
	v_lshlrev_b32_e32 v3, 4, v0
	s_mul_i32 s4, s2, 0xc000
	v_add_f32_dpp v1, v1, v1 row_ror:8 row_mask:0xf bank_mask:0xf bound_ctrl:1
	s_mul_hi_u32 s5, s2, 0xc000
	s_add_u32 s4, s10, s4
	v_add_f32_dpp v1, v1, v1 row_ror:4 row_mask:0xf bank_mask:0xf bound_ctrl:1
	s_addc_u32 s5, s11, s5
	v_add_u32_e32 v30, 0x670, v3
	v_add_f32_dpp v1, v1, v1 row_ror:2 row_mask:0xf bank_mask:0xf bound_ctrl:1
	v_mov_b32_e32 v22, s4
	v_mov_b32_e32 v23, s5
	v_add_f32_dpp v1, v1, v1 row_ror:1 row_mask:0xf bank_mask:0xf bound_ctrl:1
	v_mov_b32_e32 v21, 0
	v_mov_b32_e32 v20, v3
	v_lshl_add_u64 v[22:23], v[22:23], 0, v[20:21]
	v_readlane_b32 s16, v1, 0
	v_readlane_b32 s18, v1, 16
	v_readlane_b32 s17, v1, 32
	v_readlane_b32 s19, v1, 48
	s_and_saveexec_b64 s[8:9], s[6:7]
	v_mov_b32_e32 v4, s18
	v_mov_b32_e32 v5, s19
	v_pk_add_f32 v[4:5], s[16:17], v[4:5]
	v_lshlrev_b32_e32 v2, 2, v39
	v_add_f32_e32 v1, v4, v5
	ds_write_b32 v2, v1 offset:1536
	s_or_b64 exec, exec, s[8:9]
	s_waitcnt lgkmcnt(0)
	s_barrier
	ds_read_b128 v[4:7], v30
	ds_read_b128 v[8:11], v30 offset:12288
	ds_read_b128 v[12:15], v30 offset:24576
	ds_read_b128 v[16:19], v30 offset:36864
	s_movk_i32 s8, 0x3000
	s_mov_b32 s9, 0
	v_lshl_add_u64 v[24:25], v[22:23], 0, s[8:9]
	s_movk_i32 s8, 0x6000
	v_lshl_add_u64 v[26:27], v[22:23], 0, s[8:9]
	s_mov_b32 s8, 0x9000
	v_lshl_add_u64 v[28:29], v[22:23], 0, s[8:9]
	s_waitcnt lgkmcnt(3)
	global_store_dwordx4 v[22:23], v[4:7], off nt
	s_waitcnt lgkmcnt(2)
	global_store_dwordx4 v[24:25], v[8:11], off nt
	s_waitcnt lgkmcnt(1)
	global_store_dwordx4 v[26:27], v[12:15], off nt
	s_waitcnt lgkmcnt(0)
	global_store_dwordx4 v[28:29], v[16:19], off nt
	s_andn2_b64 exec, exec, s[0:1]
	s_cbranch_execz .Lkf_end
	v_mov_b32_e32 v1, 0
	ds_read_b128 v[2:5], v1 offset:1536
	ds_read_b128 v[6:9], v1 offset:1552
	ds_read_b128 v[10:13], v1 offset:1568
	s_ashr_i32 s3, s2, 31
	s_lshl_b64 s[4:5], s[2:3], 2
	s_add_u32 s4, s12, s4
	s_addc_u32 s5, s13, s5
	s_waitcnt lgkmcnt(2)
	v_add_f32_e32 v2, 0, v2
	v_add_f32_e32 v2, v2, v3
	v_add_f32_e32 v2, v2, v4
	v_add_f32_e32 v2, v2, v5
	s_waitcnt lgkmcnt(1)
	v_add_f32_e32 v2, v2, v6
	v_add_f32_e32 v2, v2, v7
	v_add_f32_e32 v2, v2, v8
	v_add_f32_e32 v2, v2, v9
	s_waitcnt lgkmcnt(0)
	v_add_f32_e32 v2, v2, v10
	v_add_f32_e32 v2, v2, v11
	v_add_f32_e32 v2, v2, v12
	v_add_f32_e32 v2, v2, v13
	global_store_dword v1, v2, s[4:5] nt
